# LN gain/bias loads hoisted out of the row loop in the layer-0 LN+router phase
# speedup vs baseline: 1.0102x; 1.0102x over previous
.LBB0_1282:
	s_cmp_lt_i32 s94, 8
	s_cselect_b64 s[0:1], -1, 0
	s_and_b64 s[20:21], s[0:1], s[4:5]
	s_andn2_b64 vcc, exec, s[20:21]
	s_cbranch_vccnz .LBB0_1336
	s_cmpk_gt_i32 s3, 0xff
	s_cbranch_scc1 .LBB0_1336
	v_readlane_b32 s4, v254, 21
	v_lshlrev_b32_e32 v114, 2, v1
	v_readlane_b32 s12, v254, 29
	v_readlane_b32 s13, v254, 30
	s_add_i32 s2, 0, 0x22800
	s_add_u32 s24, s92, 0x300000
	s_addc_u32 s25, s93, 0
	s_add_u32 s26, s92, 0x380000
	v_and_b32_e32 v9, 15, v0
	global_load_dword v115, v114, s[12:13]
	s_addc_u32 s27, s93, 0
	v_or_b32_e32 v2, 32, v9
	s_add_u32 s42, s92, 0x400000
	v_min_u32_e32 v15, 33, v2
	v_lshlrev_b32_e32 v2, 12, v9
	v_mov_b32_e32 v3, 0
	s_addc_u32 s43, s93, 0
	v_readlane_b32 s0, v254, 2
	v_lshl_add_u64 v[4:5], s[92:93], 0, v[2:3]
	v_lshlrev_b32_e32 v2, 4, v1
	v_or_b32_e32 v10, 0x400, v114
	s_cmpk_lt_u32 s0, 0x880
	v_lshl_add_u64 v[118:119], s[80:81], 0, v[2:3]
	v_lshl_add_u64 v[120:121], s[82:83], 0, v[2:3]
	v_lshlrev_b32_e32 v2, 2, v10
	v_or_b32_e32 v12, 0x500, v114
	s_cselect_b64 s[44:45], -1, 0
	s_lshl_b32 s22, s74, 8
	s_mov_b64 s[0:1], 0x280000
	v_lshl_add_u64 v[122:123], s[80:81], 0, v[2:3]
	v_lshl_add_u64 v[124:125], s[82:83], 0, v[2:3]
	v_lshlrev_b32_e32 v2, 2, v12
	v_or_b32_e32 v14, 0x600, v114
	v_lshl_add_u64 v[116:117], v[4:5], 0, s[0:1]
	v_lshl_add_u64 v[126:127], s[80:81], 0, v[2:3]
	v_lshl_add_u64 v[128:129], s[82:83], 0, v[2:3]
	v_lshlrev_b32_e32 v2, 2, v14
	v_or_b32_e32 v16, 0x700, v114
	s_add_u32 s34, s92, 0x100000
	s_mul_i32 s1, s74, 0x1010
	v_lshl_add_u64 v[130:131], s[80:81], 0, v[2:3]
	v_lshl_add_u64 v[132:133], s[82:83], 0, v[2:3]
	v_lshlrev_b32_e32 v2, 2, v16
	s_addc_u32 s35, s93, 0
	s_add_i32 s1, s1, 0
	v_lshrrev_b32_e32 v11, 4, v1
	v_readlane_b32 s18, v254, 35
	v_readlane_b32 s19, v254, 36
	s_mul_i32 s0, s74, 0x3000
	v_lshl_add_u64 v[134:135], s[80:81], 0, v[2:3]
	v_lshl_add_u64 v[136:137], s[82:83], 0, v[2:3]
	v_and_b32_e32 v2, 56, v0
	v_lshl_add_u32 v144, v1, 3, s1
	s_lshl_b32 s1, s74, 9
	v_lshl_or_b32 v5, v11, 10, s0
	v_cmp_eq_u32_e64 s[18:19], 56, v2
	s_movk_i32 s0, 0x1010
	v_mov_b32_e32 v2, s1
	v_lshl_or_b32 v145, v11, 3, s22
	v_mad_u32_u24 v3, v15, s0, v2
	v_and_b32_e32 v11, 48, v1
	v_mad_u32_u24 v2, v9, s0, v2
	v_add_u32_e32 v7, s2, v114
	v_lshl_add_u32 v13, v9, 2, 0
	v_readlane_b32 s5, v254, 22
	v_readlane_b32 s6, v254, 23
	v_readlane_b32 s7, v254, 24
	v_readlane_b32 s8, v254, 25
	v_readlane_b32 s9, v254, 26
	v_readlane_b32 s10, v254, 27
	v_readlane_b32 s11, v254, 28
	v_readlane_b32 s14, v254, 31
	v_readlane_b32 s15, v254, 32
	v_readlane_b32 s16, v254, 33
	v_readlane_b32 s17, v254, 34
	v_or_b32_e32 v4, 0x100, v114
	v_or_b32_e32 v6, 0x200, v114
	v_or_b32_e32 v8, 0x300, v114
	s_mul_i32 s36, s3, 34
	v_readlane_b32 s28, v254, 0
	v_add3_u32 v147, v2, v11, 0
	v_mbcnt_lo_u32_b32 v2, -1, 0
	s_mov_b32 s23, 0
	v_cmp_gt_u32_e64 s[4:5], 64, v0
	v_add_u32_e32 v139, 0, v114
	v_and_b32_e32 v142, 7, v0
	v_cmp_lt_u32_e64 s[6:7], 7, v1
	v_cmp_lt_u32_e64 s[8:9], 15, v1
	v_cmp_lt_u32_e64 s[10:11], 23, v1
	v_cmp_lt_u32_e64 s[12:13], 31, v1
	v_cmp_lt_u32_e64 s[14:15], 39, v1
	v_cmp_lt_u32_e64 s[16:17], 47, v1
	v_lshl_add_u32 v143, v0, 2, s2
	s_mul_i32 s37, s28, 34
	s_add_i32 s46, s74, s36
	v_lshlrev_b32_e32 v138, 3, v1
	v_add3_u32 v146, v3, v11, 0
	v_lshlrev_b32_e32 v148, 2, v4
	v_lshlrev_b32_e32 v149, 2, v6
	v_lshlrev_b32_e32 v150, 2, v8
	v_lshlrev_b32_e32 v151, 2, v10
	v_lshlrev_b32_e32 v152, 2, v12
	v_lshlrev_b32_e32 v153, 2, v14
	v_lshlrev_b32_e32 v154, 2, v16
	s_mov_b32 s38, 0xffff0000
	v_mov_b32_e32 v155, 0x358637bd
	s_movk_i32 s39, 0x7fff
	s_mov_b32 s40, 0xc3e00000
	s_mov_b32 s41, 0x10000
	s_mov_b32 s48, 0x20000
	s_mov_b32 s49, 0x30000
	v_add_u32_e32 v156, v13, v5
	v_add_u32_e32 v157, s22, v7
	v_mbcnt_hi_u32_b32 v158, -1, v2
	v_mov_b32_e32 v159, 1
	v_mov_b32_e32 v160, 0x43e00000
	v_mov_b32_e32 v161, 0x7f800000
	v_mov_b32_e32 v162, 0xff800000
	s_mov_b32 s51, s3
	v_readlane_b32 s29, v254, 1
	global_load_dwordx4 v[196:199], v[118:119], off
	global_load_dwordx4 v[200:203], v[120:121], off
	global_load_dwordx4 v[204:207], v[118:119], off offset:1024
	global_load_dwordx4 v[208:211], v[120:121], off offset:1024
	global_load_dwordx4 v[214:217], v[118:119], off offset:2048
	global_load_dwordx4 v[218:221], v[120:121], off offset:2048
	global_load_dwordx4 v[222:225], v[118:119], off offset:3072
	global_load_dwordx4 v[226:229], v[120:121], off offset:3072
	global_load_dwordx4 v[230:233], v[122:123], off
	global_load_dwordx4 v[234:237], v[124:125], off
	global_load_dwordx4 v[238:241], v[126:127], off
	global_load_dwordx4 v[242:245], v[130:131], off
	global_load_dwordx4 v[250:253], v[134:135], off
	global_load_dwordx4 v[118:121], v[128:129], off
	global_load_dwordx4 v[122:125], v[132:133], off
	global_load_dwordx4 v[126:129], v[136:137], off
	s_branch .LBB0_1286

.LBB0_1290:
	s_waitcnt vmcnt(0)
	v_lshlrev_b32_e32 v92, 16, v86
	v_and_b32_e32 v93, 0xffff0000, v86
	v_lshlrev_b32_e32 v98, 16, v87
	v_and_b32_e32 v99, 0xffff0000, v87
	v_add_f32_e32 v86, v92, v93
	v_add_f32_e32 v87, v98, v99
	v_lshlrev_b32_e32 v100, 16, v84
	v_and_b32_e32 v101, 0xffff0000, v84
	v_lshlrev_b32_e32 v102, 16, v85
	v_and_b32_e32 v103, 0xffff0000, v85
	v_add_f32_e32 v86, v86, v87
	v_add_f32_e32 v84, v100, v101
	v_add_f32_e32 v85, v102, v103
	v_lshlrev_b32_e32 v104, 16, v82
	v_and_b32_e32 v105, 0xffff0000, v82
	v_lshlrev_b32_e32 v106, 16, v83
	v_and_b32_e32 v107, 0xffff0000, v83
	v_add_f32_e32 v86, 0, v86
	v_add_f32_e32 v84, v84, v85
	v_add_f32_e32 v82, v104, v105
	v_add_f32_e32 v83, v106, v107
	v_lshlrev_b32_e32 v94, 16, v80
	v_and_b32_e32 v95, 0xffff0000, v80
	v_lshlrev_b32_e32 v96, 16, v81
	v_and_b32_e32 v97, 0xffff0000, v81
	v_add_f32_e32 v84, v86, v84
	v_add_f32_e32 v82, v82, v83
	v_add_f32_e32 v80, v94, v95
	v_add_f32_e32 v81, v96, v97
	v_lshlrev_b32_e32 v86, 16, v76
	v_and_b32_e32 v87, 0xffff0000, v76
	v_lshlrev_b32_e32 v88, 16, v77
	v_and_b32_e32 v89, 0xffff0000, v77
	v_add_f32_e32 v82, v84, v82
	v_add_f32_e32 v80, v80, v81
	v_add_f32_e32 v76, v86, v87
	v_add_f32_e32 v77, v88, v89
	v_add_f32_e32 v80, v82, v80
	v_add_f32_e32 v76, v76, v77
	v_add_f32_e32 v76, v80, v76
	v_lshlrev_b32_e32 v80, 16, v72
	v_and_b32_e32 v81, 0xffff0000, v72
	v_lshlrev_b32_e32 v82, 16, v73
	v_and_b32_e32 v83, 0xffff0000, v73
	v_add_f32_e32 v72, v80, v81
	v_add_f32_e32 v73, v82, v83
	v_add_f32_e32 v72, v72, v73
	v_add_f32_e32 v76, v76, v72
	v_lshlrev_b32_e32 v72, 16, v74
	v_and_b32_e32 v73, 0xffff0000, v74
	v_lshlrev_b32_e32 v74, 16, v75
	v_and_b32_e32 v75, 0xffff0000, v75
	v_add_f32_e32 v77, v72, v73
	v_add_f32_e32 v84, v74, v75
	v_add_f32_e32 v77, v77, v84
	v_add_f32_e32 v84, v76, v77
	v_lshlrev_b32_e32 v76, 16, v78
	v_and_b32_e32 v77, 0xffff0000, v78
	v_lshlrev_b32_e32 v78, 16, v79
	v_and_b32_e32 v79, 0xffff0000, v79
	v_add_f32_e32 v85, v76, v77
	v_add_f32_e32 v90, v78, v79
	v_add_f32_e32 v85, v85, v90
	v_add_f32_e32 v84, v84, v85
	ds_bpermute_b32 v85, v91, v84
	s_mov_b32 s0, 0x800000
	v_mov_b32_e32 v176, 0
	s_add_i32 s22, s30, 8
	s_cmp_gt_u32 s30, 25
	s_waitcnt lgkmcnt(0)
	v_add_f32_e32 v84, v84, v85
	ds_bpermute_b32 v85, v108, v84
	s_waitcnt lgkmcnt(0)
	v_add_f32_e32 v84, v84, v85
	ds_bpermute_b32 v85, v109, v84
	s_waitcnt lgkmcnt(0)
	v_add_f32_e32 v84, v84, v85
	ds_bpermute_b32 v85, v110, v84
	s_waitcnt lgkmcnt(0)
	v_add_f32_e32 v84, v84, v85
	ds_bpermute_b32 v85, v111, v84
	s_waitcnt lgkmcnt(0)
	v_add_f32_e32 v84, v84, v85
	ds_bpermute_b32 v85, v112, v84
	s_waitcnt lgkmcnt(0)
	v_add_f32_e32 v90, v84, v85
	v_fmac_f32_e32 v93, 0xba000000, v90
	v_fmac_f32_e32 v101, 0xba000000, v90
	v_fmac_f32_e32 v99, 0xba000000, v90
	v_fmac_f32_e32 v92, 0xba000000, v90
	v_fmac_f32_e32 v103, 0xba000000, v90
	v_fmac_f32_e32 v100, 0xba000000, v90
	v_mov_b32_e32 v140, v93
	v_mov_b32_e32 v141, v101
	v_fmac_f32_e32 v98, 0xba000000, v90
	v_fmac_f32_e32 v102, 0xba000000, v90
	v_mov_b32_e32 v84, v92
	v_mov_b32_e32 v85, v100
	v_pk_mul_f32 v[140:141], v[140:141], v[140:141]
	v_mov_b32_e32 v164, v99
	v_mov_b32_e32 v165, v103
	v_pk_fma_f32 v[84:85], v[84:85], v[84:85], v[140:141]
	v_mov_b32_e32 v140, v98
	v_mov_b32_e32 v141, v102
	v_pk_mul_f32 v[164:165], v[164:165], v[164:165]
	v_fmac_f32_e32 v105, 0xba000000, v90
	v_pk_fma_f32 v[140:141], v[140:141], v[140:141], v[164:165]
	v_fmac_f32_e32 v104, 0xba000000, v90
	v_pk_add_f32 v[84:85], v[84:85], v[140:141]
	v_fmac_f32_e32 v107, 0xba000000, v90
	v_fmac_f32_e32 v106, 0xba000000, v90
	v_pk_add_f32 v[84:85], v[84:85], v[84:85] op_sel_hi:[0,1]
	v_pk_mul_f32 v[140:141], v[106:107], v[106:107]
	v_pk_mul_f32 v[164:165], v[104:105], v[104:105]
	v_fmac_f32_e32 v94, 0xba000000, v90
	v_pk_mov_b32 v[166:167], v[164:165], v[140:141] op_sel:[1,0]
	v_mov_b32_e32 v165, v141
	v_fmac_f32_e32 v95, 0xba000000, v90
	v_fmac_f32_e32 v96, 0xba000000, v90
	v_mul_f32_e32 v84, v94, v94
	v_pk_add_f32 v[140:141], v[166:167], v[164:165]
	v_fmac_f32_e32 v97, 0xba000000, v90
	v_pk_fma_f32 v[164:165], v[94:95], v[94:95], v[84:85] op_sel_hi:[1,1,0]
	v_mul_f32_e32 v84, v96, v96
	v_pk_add_f32 v[140:141], v[140:141], v[140:141] op_sel_hi:[0,1]
	v_pk_fma_f32 v[166:167], v[96:97], v[96:97], v[84:85] op_sel_hi:[1,1,0]
	v_fmac_f32_e32 v89, 0xba000000, v90
	v_fmac_f32_e32 v88, 0xba000000, v90
	v_fmac_f32_e32 v87, 0xba000000, v90
	v_fmac_f32_e32 v86, 0xba000000, v90
	v_mul_f32_e32 v164, v86, v86
	v_mul_f32_e32 v166, v87, v87
	v_mul_f32_e32 v140, v88, v88
	v_mul_f32_e32 v84, v89, v89
	v_pk_add_f32 v[164:165], v[164:165], v[166:167]
	v_pk_add_f32 v[84:85], v[140:141], v[84:85]
	v_fmac_f32_e32 v81, 0xba000000, v90
	v_pk_add_f32 v[84:85], v[164:165], v[84:85]
	v_fmac_f32_e32 v80, 0xba000000, v90
	v_fmac_f32_e32 v83, 0xba000000, v90
	v_fmac_f32_e32 v82, 0xba000000, v90
	v_pk_add_f32 v[84:85], v[84:85], v[84:85] op_sel_hi:[0,1]
	v_pk_mul_f32 v[140:141], v[82:83], v[82:83]
	v_pk_mul_f32 v[172:173], v[80:81], v[80:81]
	v_fmac_f32_e32 v72, 0xba000000, v90
	v_pk_mov_b32 v[174:175], v[172:173], v[140:141] op_sel:[1,0]
	v_mov_b32_e32 v173, v141
	v_fmac_f32_e32 v73, 0xba000000, v90
	v_fmac_f32_e32 v74, 0xba000000, v90
	v_mul_f32_e32 v84, v72, v72
	v_pk_add_f32 v[140:141], v[174:175], v[172:173]
	v_fmac_f32_e32 v75, 0xba000000, v90
	v_pk_fma_f32 v[172:173], v[72:73], v[72:73], v[84:85] op_sel_hi:[1,1,0]
	v_mul_f32_e32 v84, v74, v74
	v_pk_add_f32 v[140:141], v[140:141], v[140:141] op_sel_hi:[0,1]
	v_pk_fma_f32 v[174:175], v[74:75], v[74:75], v[84:85] op_sel_hi:[1,1,0]
	v_fmac_f32_e32 v79, 0xba000000, v90
	v_fmac_f32_e32 v78, 0xba000000, v90
	v_fmac_f32_e32 v77, 0xba000000, v90
	v_fmac_f32_e32 v76, 0xba000000, v90
	v_mul_f32_e32 v172, v76, v76
	v_mul_f32_e32 v174, v77, v77
	v_mul_f32_e32 v140, v78, v78
	v_mul_f32_e32 v84, v79, v79
	v_pk_add_f32 v[172:173], v[172:173], v[174:175]
	v_pk_add_f32 v[84:85], v[140:141], v[84:85]
	s_nop 0
	v_pk_add_f32 v[84:85], v[172:173], v[84:85]
	s_nop 0
	v_add_f32_e32 v84, v84, v85
	ds_bpermute_b32 v85, v91, v84
	s_waitcnt lgkmcnt(0)
	v_add_f32_e32 v84, v84, v85
	ds_bpermute_b32 v85, v108, v84
	s_waitcnt lgkmcnt(0)
	v_add_f32_e32 v84, v84, v85
	ds_bpermute_b32 v85, v109, v84
	s_waitcnt lgkmcnt(0)
	v_add_f32_e32 v84, v84, v85
	ds_bpermute_b32 v85, v110, v84
	s_waitcnt lgkmcnt(0)
	v_add_f32_e32 v84, v84, v85
	ds_bpermute_b32 v85, v111, v84
	s_waitcnt lgkmcnt(0)
	v_add_f32_e32 v84, v84, v85
	ds_bpermute_b32 v85, v112, v84
	s_waitcnt lgkmcnt(0)
	v_add_f32_e32 v84, v84, v85
	v_fmamk_f32 v84, v84, 0x3a000000, v155
	v_mul_f32_e32 v85, 0x4b800000, v84
	v_cmp_gt_f32_e32 vcc, s0, v84
	s_mov_b64 s[0:1], 0x34000000
	s_nop 0
	v_cndmask_b32_e32 v84, v84, v85, vcc
	v_rsq_f32_e32 v90, v84
	v_lshl_add_u64 v[84:85], v[70:71], 0, s[0:1]
	s_mov_b32 s0, 0x38400000
	v_mul_f32_e32 v140, 0x45800000, v90
	v_cndmask_b32_e32 v90, v90, v140, vcc
	v_pk_mul_f32 v[92:93], v[92:93], v[90:91] op_sel_hi:[1,0]
	v_pk_mul_f32 v[98:99], v[98:99], v[90:91] op_sel_hi:[1,0]
	v_pk_fma_f32 v[92:93], v[196:197], v[92:93], v[200:201]
	v_pk_fma_f32 v[98:99], v[198:199], v[98:99], v[202:203]
	v_bfe_u32 v140, v92, 16, 1
	v_add3_u32 v140, v92, v140, s39
	v_bfe_u32 v141, v93, 16, 1
	v_lshrrev_b32_e32 v140, 16, v140
	v_add3_u32 v141, v93, v141, s39
	v_and_or_b32 v140, v141, s38, v140
	v_bfe_u32 v141, v98, 16, 1
	v_add3_u32 v141, v98, v141, s39
	v_bfe_u32 v163, v99, 16, 1
	v_lshrrev_b32_e32 v141, 16, v141
	v_add3_u32 v163, v99, v163, s39
	v_and_or_b32 v141, v163, s38, v141
	v_pk_fma_f32 v[92:93], v[6:7], v[92:93], v[2:3]
	global_store_dwordx2 v[84:85], v[140:141], off
	v_med3_f32 v84, v92, s40, v160
	v_med3_f32 v85, v93, s40, v160
	v_mov_b32_e32 v140, 0
	v_cvt_pk_fp8_f32 v140, v84, v85
	v_pk_fma_f32 v[98:99], v[8:9], v[98:99], v[4:5]
	v_pk_mul_f32 v[100:101], v[100:101], v[90:91] op_sel_hi:[1,0]
	v_med3_f32 v84, v98, s40, v160
	v_med3_f32 v85, v99, s40, v160
	v_cvt_pk_fp8_f32 v140, v84, v85 op_sel:[0,0,1]
	v_lshl_add_u64 v[84:85], s[92:93], 0, v[66:67]
	v_add_co_u32_e32 v84, vcc, s0, v84
	v_pk_mul_f32 v[102:103], v[102:103], v[90:91] op_sel_hi:[1,0]
	s_nop 0
	v_addc_co_u32_e32 v85, vcc, 0, v85, vcc
	global_store_dword v[84:85], v140, off
	s_mov_b64 s[0:1], 0x34000200
	v_lshl_add_u64 v[140:141], v[70:71], 0, s[0:1]
	v_pk_mul_f32 v[104:105], v[104:105], v[90:91] op_sel_hi:[1,0]
	v_pk_mul_f32 v[106:107], v[106:107], v[90:91] op_sel_hi:[1,0]
	s_mov_b64 s[0:1], 0x34000400
	v_pk_mul_f32 v[94:95], v[94:95], v[90:91] op_sel_hi:[1,0]
	v_pk_mul_f32 v[96:97], v[96:97], v[90:91] op_sel_hi:[1,0]
	v_pk_mul_f32 v[86:87], v[86:87], v[90:91] op_sel_hi:[1,0]
	v_pk_mul_f32 v[88:89], v[88:89], v[90:91] op_sel_hi:[1,0]
	v_pk_mul_f32 v[80:81], v[80:81], v[90:91] op_sel_hi:[1,0]
	v_pk_mul_f32 v[82:83], v[82:83], v[90:91] op_sel_hi:[1,0]
	v_pk_mul_f32 v[72:73], v[72:73], v[90:91] op_sel_hi:[1,0]
	v_pk_mul_f32 v[74:75], v[74:75], v[90:91] op_sel_hi:[1,0]
	v_pk_mul_f32 v[172:173], v[76:77], v[90:91] op_sel_hi:[1,0]
	v_and_b32_sdwa v76, v98, v159 dst_sel:DWORD dst_unused:UNUSED_PAD src0_sel:WORD_1 src1_sel:DWORD
	v_and_b32_sdwa v77, v92, v159 dst_sel:DWORD dst_unused:UNUSED_PAD src0_sel:WORD_1 src1_sel:DWORD
	v_pk_mul_f32 v[174:175], v[78:79], v[90:91] op_sel_hi:[1,0]
	v_add3_u32 v90, v92, v77, s39
	v_add3_u32 v92, v98, v76, s39
	v_and_b32_sdwa v78, v99, v159 dst_sel:DWORD dst_unused:UNUSED_PAD src0_sel:WORD_1 src1_sel:DWORD
	v_add3_u32 v98, v99, v78, s39
	v_and_b32_sdwa v79, v93, v159 dst_sel:DWORD dst_unused:UNUSED_PAD src0_sel:WORD_1 src1_sel:DWORD
	v_add3_u32 v93, v93, v79, s39
	v_and_b32_e32 v98, 0xffff0000, v98
	v_and_b32_e32 v99, 0xffff0000, v93
	v_or_b32_sdwa v93, v98, v92 dst_sel:DWORD dst_unused:UNUSED_PAD src0_sel:DWORD src1_sel:WORD_1
	v_or_b32_sdwa v92, v99, v90 dst_sel:DWORD dst_unused:UNUSED_PAD src0_sel:DWORD src1_sel:WORD_1
	v_pk_fma_f32 v[100:101], v[204:205], v[100:101], v[208:209]
	v_pk_fma_f32 v[166:167], v[206:207], v[102:103], v[210:211]
	v_bfe_u32 v102, v100, 16, 1
	v_add3_u32 v102, v100, v102, s39
	v_bfe_u32 v103, v101, 16, 1
	v_lshrrev_b32_e32 v102, 16, v102
	v_add3_u32 v103, v101, v103, s39
	v_and_or_b32 v164, v103, s38, v102
	v_bfe_u32 v102, v166, 16, 1
	v_add3_u32 v102, v166, v102, s39
	v_pk_fma_f32 v[100:101], v[14:15], v[100:101], v[10:11]
	v_lshrrev_b32_e32 v163, 16, v102
	v_med3_f32 v102, v100, s40, v160
	v_med3_f32 v103, v101, s40, v160
	v_mov_b32_e32 v168, 0
	v_cvt_pk_fp8_f32 v168, v102, v103
	v_pk_fma_f32 v[102:103], v[16:17], v[166:167], v[12:13]
	v_bfe_u32 v165, v167, 16, 1
	v_med3_f32 v166, v102, s40, v160
	v_med3_f32 v169, v103, s40, v160
	v_cvt_pk_fp8_f32 v168, v166, v169 op_sel:[0,0,1]
	v_add3_u32 v165, v167, v165, s39
	v_and_or_b32 v165, v165, s38, v163
	global_store_dwordx2 v[140:141], v[164:165], off
	global_store_dword v[84:85], v168, off offset:256
	v_mov_b32_e32 v163, 0
	v_lshl_add_u64 v[140:141], v[70:71], 0, s[0:1]
	s_mov_b64 s[0:1], 0x34000600
	v_and_b32_sdwa v98, v100, v159 dst_sel:DWORD dst_unused:UNUSED_PAD src0_sel:WORD_1 src1_sel:DWORD
	v_and_b32_sdwa v99, v103, v159 dst_sel:DWORD dst_unused:UNUSED_PAD src0_sel:WORD_1 src1_sel:DWORD
	v_and_b32_sdwa v90, v102, v159 dst_sel:DWORD dst_unused:UNUSED_PAD src0_sel:WORD_1 src1_sel:DWORD
	v_add3_u32 v98, v100, v98, s39
	v_add3_u32 v99, v103, v99, s39
	v_add3_u32 v90, v102, v90, s39
	v_and_b32_e32 v99, 0xffff0000, v99
	v_or_b32_sdwa v99, v99, v90 dst_sel:DWORD dst_unused:UNUSED_PAD src0_sel:DWORD src1_sel:WORD_1
	v_pk_fma_f32 v[164:165], v[214:215], v[104:105], v[218:219]
	v_pk_fma_f32 v[166:167], v[216:217], v[106:107], v[220:221]
	v_bfe_u32 v168, v164, 16, 1
	v_bfe_u32 v169, v165, 16, 1
	v_pk_fma_f32 v[106:107], v[22:23], v[164:165], v[18:19]
	v_add3_u32 v164, v164, v168, s39
	v_add3_u32 v165, v165, v169, s39
	v_med3_f32 v168, v106, s40, v160
	v_med3_f32 v169, v107, s40, v160
	v_cvt_pk_fp8_f32 v163, v168, v169
	v_bfe_u32 v170, v166, 16, 1
	v_pk_fma_f32 v[104:105], v[24:25], v[166:167], v[20:21]
	v_add3_u32 v166, v166, v170, s39
	v_med3_f32 v170, v104, s40, v160
	v_med3_f32 v168, v105, s40, v160
	v_bfe_u32 v171, v167, 16, 1
	v_cvt_pk_fp8_f32 v163, v170, v168 op_sel:[0,0,1]
	v_add3_u32 v167, v167, v171, s39
	v_lshrrev_b32_e32 v164, 16, v164
	v_lshrrev_b32_e32 v166, 16, v166
	v_and_or_b32 v164, v165, s38, v164
	v_and_or_b32 v165, v167, s38, v166
	global_store_dwordx2 v[140:141], v[164:165], off
	global_store_dword v[84:85], v163, off offset:512
	v_mov_b32_e32 v163, 0
	v_lshl_add_u64 v[140:141], v[70:71], 0, s[0:1]
	s_mov_b64 s[0:1], 0x34000800
	v_and_b32_sdwa v90, v104, v159 dst_sel:DWORD dst_unused:UNUSED_PAD src0_sel:WORD_1 src1_sel:DWORD
	v_add3_u32 v90, v104, v90, s39
	v_pk_fma_f32 v[164:165], v[222:223], v[94:95], v[226:227]
	v_pk_fma_f32 v[166:167], v[224:225], v[96:97], v[228:229]
	v_bfe_u32 v168, v164, 16, 1
	v_bfe_u32 v169, v165, 16, 1
	v_pk_fma_f32 v[96:97], v[30:31], v[164:165], v[26:27]
	v_add3_u32 v164, v164, v168, s39
	v_add3_u32 v165, v165, v169, s39
	v_med3_f32 v168, v96, s40, v160
	v_med3_f32 v169, v97, s40, v160
	v_cvt_pk_fp8_f32 v163, v168, v169
	v_bfe_u32 v170, v166, 16, 1
	v_pk_fma_f32 v[94:95], v[32:33], v[166:167], v[28:29]
	v_add3_u32 v166, v166, v170, s39
	v_med3_f32 v170, v94, s40, v160
	v_med3_f32 v168, v95, s40, v160
	v_bfe_u32 v171, v167, 16, 1
	v_cvt_pk_fp8_f32 v163, v170, v168 op_sel:[0,0,1]
	v_add3_u32 v167, v167, v171, s39
	v_lshrrev_b32_e32 v164, 16, v164
	v_lshrrev_b32_e32 v166, 16, v166
	v_and_or_b32 v164, v165, s38, v164
	v_and_or_b32 v165, v167, s38, v166
	global_store_dwordx2 v[140:141], v[164:165], off
	global_store_dword v[84:85], v163, off offset:768
	v_mov_b32_e32 v163, 0
	v_lshl_add_u64 v[140:141], v[70:71], 0, s[0:1]
	s_mov_b64 s[0:1], 0x34000a00
	v_pk_fma_f32 v[164:165], v[86:87], v[230:231], v[234:235]
	v_pk_fma_f32 v[166:167], v[88:89], v[232:233], v[236:237]
	v_bfe_u32 v168, v164, 16, 1
	v_bfe_u32 v169, v165, 16, 1
	v_pk_fma_f32 v[88:89], v[38:39], v[164:165], v[34:35]
	v_add3_u32 v164, v164, v168, s39
	v_add3_u32 v165, v165, v169, s39
	v_med3_f32 v168, v88, s40, v160
	v_med3_f32 v169, v89, s40, v160
	v_cvt_pk_fp8_f32 v163, v168, v169
	v_bfe_u32 v170, v166, 16, 1
	v_pk_fma_f32 v[86:87], v[40:41], v[166:167], v[36:37]
	v_add3_u32 v166, v166, v170, s39
	v_med3_f32 v170, v86, s40, v160
	v_med3_f32 v168, v87, s40, v160
	v_bfe_u32 v171, v167, 16, 1
	v_cvt_pk_fp8_f32 v163, v170, v168 op_sel:[0,0,1]
	v_add3_u32 v167, v167, v171, s39
	v_lshrrev_b32_e32 v164, 16, v164
	v_lshrrev_b32_e32 v166, 16, v166
	v_and_or_b32 v164, v165, s38, v164
	v_and_or_b32 v165, v167, s38, v166
	global_store_dwordx2 v[140:141], v[164:165], off
	global_store_dword v[84:85], v163, off offset:1024
	v_mov_b32_e32 v163, 0
	v_lshl_add_u64 v[140:141], v[70:71], 0, s[0:1]
	s_mov_b64 s[0:1], 0x34000c00
	v_pk_fma_f32 v[80:81], v[80:81], v[238:239], v[118:119]
	v_pk_fma_f32 v[82:83], v[82:83], v[240:241], v[120:121]
	v_bfe_u32 v164, v80, 16, 1
	v_bfe_u32 v165, v81, 16, 1
	v_pk_fma_f32 v[170:171], v[46:47], v[80:81], v[42:43]
	v_add3_u32 v80, v80, v164, s39
	v_add3_u32 v81, v81, v165, s39
	v_med3_f32 v164, v170, s40, v160
	v_med3_f32 v165, v171, s40, v160
	v_cvt_pk_fp8_f32 v163, v164, v165
	v_bfe_u32 v166, v82, 16, 1
	v_pk_fma_f32 v[168:169], v[48:49], v[82:83], v[44:45]
	v_add3_u32 v82, v82, v166, s39
	v_med3_f32 v166, v168, s40, v160
	v_med3_f32 v164, v169, s40, v160
	v_bfe_u32 v167, v83, 16, 1
	v_cvt_pk_fp8_f32 v163, v166, v164 op_sel:[0,0,1]
	v_add3_u32 v83, v83, v167, s39
	v_lshrrev_b32_e32 v80, 16, v80
	v_lshrrev_b32_e32 v82, 16, v82
	v_and_or_b32 v80, v81, s38, v80
	v_and_or_b32 v81, v83, s38, v82
	global_store_dwordx2 v[140:141], v[80:81], off
	global_store_dword v[84:85], v163, off offset:1280
	v_mov_b32_e32 v163, 0
	v_lshl_add_u64 v[140:141], v[70:71], 0, s[0:1]
	s_mov_b64 s[0:1], 0x34000e00
	v_lshl_add_u64 v[70:71], v[70:71], 0, s[0:1]
	s_mov_b64 s[0:1], 0x4000
	v_lshl_add_u64 v[66:67], v[66:67], 0, s[0:1]
	s_mov_b64 s[0:1], 0x8000
	v_lshl_add_u64 v[68:69], v[68:69], 0, s[0:1]
	v_pk_fma_f32 v[72:73], v[72:73], v[242:243], v[122:123]
	v_pk_fma_f32 v[74:75], v[74:75], v[244:245], v[124:125]
	v_bfe_u32 v76, v72, 16, 1
	v_bfe_u32 v77, v73, 16, 1
	v_pk_fma_f32 v[82:83], v[54:55], v[72:73], v[50:51]
	v_add3_u32 v72, v72, v76, s39
	v_add3_u32 v73, v73, v77, s39
	v_med3_f32 v76, v82, s40, v160
	v_med3_f32 v77, v83, s40, v160
	v_cvt_pk_fp8_f32 v163, v76, v77
	v_bfe_u32 v78, v74, 16, 1
	v_pk_fma_f32 v[80:81], v[56:57], v[74:75], v[52:53]
	v_add3_u32 v74, v74, v78, s39
	v_med3_f32 v78, v80, s40, v160
	v_med3_f32 v76, v81, s40, v160
	v_bfe_u32 v79, v75, 16, 1
	v_cvt_pk_fp8_f32 v163, v78, v76 op_sel:[0,0,1]
	v_add3_u32 v75, v75, v79, s39
	v_lshrrev_b32_e32 v72, 16, v72
	v_lshrrev_b32_e32 v74, 16, v74
	v_and_or_b32 v72, v73, s38, v72
	v_and_or_b32 v73, v75, s38, v74
	global_store_dwordx2 v[140:141], v[72:73], off
	global_store_dword v[84:85], v163, off offset:1536
	v_and_b32_sdwa v140, v101, v159 dst_sel:DWORD dst_unused:UNUSED_PAD src0_sel:WORD_1 src1_sel:DWORD
	v_add3_u32 v100, v101, v140, s39
	v_and_b32_e32 v100, 0xffff0000, v100
	v_or_b32_sdwa v98, v100, v98 dst_sel:DWORD dst_unused:UNUSED_PAD src0_sel:DWORD src1_sel:WORD_1
	ds_write2st64_b64 v113, v[92:93], v[98:99] offset1:1
	v_and_b32_sdwa v93, v105, v159 dst_sel:DWORD dst_unused:UNUSED_PAD src0_sel:WORD_1 src1_sel:DWORD
	v_and_b32_sdwa v98, v107, v159 dst_sel:DWORD dst_unused:UNUSED_PAD src0_sel:WORD_1 src1_sel:DWORD
	v_add3_u32 v93, v105, v93, s39
	v_and_b32_sdwa v92, v106, v159 dst_sel:DWORD dst_unused:UNUSED_PAD src0_sel:WORD_1 src1_sel:DWORD
	v_add3_u32 v98, v107, v98, s39
	v_and_b32_e32 v93, 0xffff0000, v93
	v_add3_u32 v92, v106, v92, s39
	v_and_b32_e32 v98, 0xffff0000, v98
	v_or_b32_sdwa v93, v93, v90 dst_sel:DWORD dst_unused:UNUSED_PAD src0_sel:DWORD src1_sel:WORD_1
	v_and_b32_sdwa v90, v94, v159 dst_sel:DWORD dst_unused:UNUSED_PAD src0_sel:WORD_1 src1_sel:DWORD
	v_and_b32_sdwa v99, v95, v159 dst_sel:DWORD dst_unused:UNUSED_PAD src0_sel:WORD_1 src1_sel:DWORD
	v_and_b32_sdwa v100, v97, v159 dst_sel:DWORD dst_unused:UNUSED_PAD src0_sel:WORD_1 src1_sel:DWORD
	v_or_b32_sdwa v92, v98, v92 dst_sel:DWORD dst_unused:UNUSED_PAD src0_sel:DWORD src1_sel:WORD_1
	v_and_b32_sdwa v98, v96, v159 dst_sel:DWORD dst_unused:UNUSED_PAD src0_sel:WORD_1 src1_sel:DWORD
	v_add3_u32 v90, v94, v90, s39
	v_add3_u32 v94, v95, v99, s39
	v_add3_u32 v95, v97, v100, s39
	v_add3_u32 v96, v96, v98, s39
	v_and_b32_e32 v94, 0xffff0000, v94
	v_and_b32_e32 v97, 0xffff0000, v95
	v_or_b32_sdwa v95, v94, v90 dst_sel:DWORD dst_unused:UNUSED_PAD src0_sel:DWORD src1_sel:WORD_1
	v_or_b32_sdwa v94, v97, v96 dst_sel:DWORD dst_unused:UNUSED_PAD src0_sel:DWORD src1_sel:WORD_1
	ds_write2st64_b64 v113, v[92:93], v[94:95] offset0:2 offset1:3
	v_and_b32_sdwa v93, v87, v159 dst_sel:DWORD dst_unused:UNUSED_PAD src0_sel:WORD_1 src1_sel:DWORD
	v_and_b32_sdwa v94, v89, v159 dst_sel:DWORD dst_unused:UNUSED_PAD src0_sel:WORD_1 src1_sel:DWORD
	v_and_b32_sdwa v90, v86, v159 dst_sel:DWORD dst_unused:UNUSED_PAD src0_sel:WORD_1 src1_sel:DWORD
	v_and_b32_sdwa v92, v88, v159 dst_sel:DWORD dst_unused:UNUSED_PAD src0_sel:WORD_1 src1_sel:DWORD
	v_add3_u32 v87, v87, v93, s39
	v_add3_u32 v89, v89, v94, s39
	v_add3_u32 v88, v88, v92, s39
	v_add3_u32 v86, v86, v90, s39
	v_and_b32_e32 v87, 0xffff0000, v87
	v_and_b32_e32 v89, 0xffff0000, v89
	v_or_b32_sdwa v87, v87, v86 dst_sel:DWORD dst_unused:UNUSED_PAD src0_sel:DWORD src1_sel:WORD_1
	v_or_b32_sdwa v86, v89, v88 dst_sel:DWORD dst_unused:UNUSED_PAD src0_sel:DWORD src1_sel:WORD_1
	v_and_b32_sdwa v89, v170, v159 dst_sel:DWORD dst_unused:UNUSED_PAD src0_sel:WORD_1 src1_sel:DWORD
	v_and_b32_sdwa v90, v169, v159 dst_sel:DWORD dst_unused:UNUSED_PAD src0_sel:WORD_1 src1_sel:DWORD
	v_and_b32_sdwa v92, v171, v159 dst_sel:DWORD dst_unused:UNUSED_PAD src0_sel:WORD_1 src1_sel:DWORD
	v_and_b32_sdwa v88, v168, v159 dst_sel:DWORD dst_unused:UNUSED_PAD src0_sel:WORD_1 src1_sel:DWORD
	v_add3_u32 v93, v170, v89, s39
	v_add3_u32 v89, v169, v90, s39
	v_add3_u32 v90, v171, v92, s39
	v_add3_u32 v88, v168, v88, s39
	v_and_b32_e32 v89, 0xffff0000, v89
	v_and_b32_e32 v90, 0xffff0000, v90
	v_or_b32_sdwa v89, v89, v88 dst_sel:DWORD dst_unused:UNUSED_PAD src0_sel:DWORD src1_sel:WORD_1
	v_or_b32_sdwa v88, v90, v93 dst_sel:DWORD dst_unused:UNUSED_PAD src0_sel:DWORD src1_sel:WORD_1
	ds_write2st64_b64 v113, v[86:87], v[88:89] offset0:4 offset1:5
	v_and_b32_sdwa v88, v81, v159 dst_sel:DWORD dst_unused:UNUSED_PAD src0_sel:WORD_1 src1_sel:DWORD
	v_and_b32_sdwa v89, v83, v159 dst_sel:DWORD dst_unused:UNUSED_PAD src0_sel:WORD_1 src1_sel:DWORD
	v_add3_u32 v81, v81, v88, s39
	v_add3_u32 v83, v83, v89, s39
	v_and_b32_sdwa v86, v80, v159 dst_sel:DWORD dst_unused:UNUSED_PAD src0_sel:WORD_1 src1_sel:DWORD
	v_and_b32_sdwa v87, v82, v159 dst_sel:DWORD dst_unused:UNUSED_PAD src0_sel:WORD_1 src1_sel:DWORD
	v_add3_u32 v82, v82, v87, s39
	v_add3_u32 v80, v80, v86, s39
	v_and_b32_e32 v81, 0xffff0000, v81
	v_and_b32_e32 v83, 0xffff0000, v83
	v_or_b32_sdwa v81, v81, v80 dst_sel:DWORD dst_unused:UNUSED_PAD src0_sel:DWORD src1_sel:WORD_1
	v_or_b32_sdwa v80, v83, v82 dst_sel:DWORD dst_unused:UNUSED_PAD src0_sel:DWORD src1_sel:WORD_1
	v_pk_fma_f32 v[72:73], v[172:173], v[250:251], v[126:127]
	v_pk_fma_f32 v[74:75], v[174:175], v[252:253], v[128:129]
	v_pk_fma_f32 v[78:79], v[58:59], v[72:73], v[62:63]
	v_bfe_u32 v82, v72, 16, 1
	v_med3_f32 v88, v78, s40, v160
	v_med3_f32 v89, v79, s40, v160
	v_cvt_pk_fp8_f32 v176, v88, v89
	v_bfe_u32 v86, v74, 16, 1
	v_bfe_u32 v87, v75, 16, 1
	v_pk_fma_f32 v[76:77], v[60:61], v[74:75], v[64:65]
	v_bfe_u32 v83, v73, 16, 1
	v_add3_u32 v72, v72, v82, s39
	v_add3_u32 v74, v74, v86, s39
	v_add3_u32 v75, v75, v87, s39
	v_and_b32_sdwa v86, v77, v159 dst_sel:DWORD dst_unused:UNUSED_PAD src0_sel:WORD_1 src1_sel:DWORD
	v_and_b32_sdwa v87, v79, v159 dst_sel:DWORD dst_unused:UNUSED_PAD src0_sel:WORD_1 src1_sel:DWORD
	v_med3_f32 v90, v76, s40, v160
	v_med3_f32 v92, v77, s40, v160
	v_add3_u32 v73, v73, v83, s39
	v_and_b32_sdwa v82, v76, v159 dst_sel:DWORD dst_unused:UNUSED_PAD src0_sel:WORD_1 src1_sel:DWORD
	v_and_b32_sdwa v83, v78, v159 dst_sel:DWORD dst_unused:UNUSED_PAD src0_sel:WORD_1 src1_sel:DWORD
	v_lshrrev_b32_e32 v72, 16, v72
	v_lshrrev_b32_e32 v74, 16, v74
	v_add3_u32 v77, v77, v86, s39
	v_add3_u32 v79, v79, v87, s39
	v_cvt_pk_fp8_f32 v176, v90, v92 op_sel:[0,0,1]
	v_add3_u32 v78, v78, v83, s39
	v_add3_u32 v76, v76, v82, s39
	v_and_or_b32 v72, v73, s38, v72
	v_and_or_b32 v73, v75, s38, v74
	v_and_b32_e32 v74, 0xffff0000, v77
	v_and_b32_e32 v75, 0xffff0000, v79
	global_store_dwordx2 v[70:71], v[72:73], off
	v_or_b32_sdwa v71, v74, v76 dst_sel:DWORD dst_unused:UNUSED_PAD src0_sel:DWORD src1_sel:WORD_1
	v_or_b32_sdwa v70, v75, v78 dst_sel:DWORD dst_unused:UNUSED_PAD src0_sel:DWORD src1_sel:WORD_1
	ds_write2st64_b64 v113, v[80:81], v[70:71] offset0:6 offset1:7
	v_add_u32_e32 v113, 0x8080, v113
	global_store_dword v[84:85], v176, off offset:1792
	s_cbranch_scc1 .LBB0_1292
	s_mov_b32 s30, s22
	s_branch .LBB0_1288
